# baseline (speedup 1.0000x reference)
.LBB1_136:
	v_add_u32_e32 v128, 16, v146
	v_lshlrev_b32_e32 v128, 8, v128
	v_and_b32_e32 v128, 0x7ff00, v128
	v_add_u32_e32 v128, v128, v144
	global_load_dwordx4 v[66:69], v128, s[22:23] offset:16
	global_load_dwordx4 v[134:137], v128, s[22:23]
	v_add_u32_e32 v128, 32, v146
	v_lshlrev_b32_e32 v128, 8, v128
	v_and_b32_e32 v128, 0x7ff00, v128
	v_add_u32_e32 v128, v128, v144
	global_load_dwordx4 v[148:151], v128, s[22:23] offset:16
	global_load_dwordx4 v[140:143], v128, s[22:23]
	s_waitcnt vmcnt(2)
	v_mul_f32_e32 v126, v115, v135
	v_mul_f32_e32 v127, v115, v134
	v_fma_f32 v118, v114, v134, -v126
	v_fma_f32 v119, v114, v135, v127
	v_mul_f32_e32 v126, v117, v137
	v_mul_f32_e32 v127, v117, v136
	v_fma_f32 v120, v116, v136, -v126
	v_fma_f32 v121, v116, v137, v127
	v_mul_f32_e32 v126, v111, v67
	v_mul_f32_e32 v127, v111, v66
	v_fma_f32 v122, v110, v66, -v126
	v_fma_f32 v123, v110, v67, v127
	v_mul_f32_e32 v126, v113, v69
	v_mul_f32_e32 v127, v113, v68
	v_fma_f32 v124, v112, v68, -v126
	v_fma_f32 v125, v112, v69, v127
	v_pk_mul_f32 v[118:119], v[138:139], v[118:119]
	v_pk_mul_f32 v[120:121], v[138:139], v[120:121]
	v_pk_mul_f32 v[122:123], v[138:139], v[122:123]
	v_pk_mul_f32 v[124:125], v[138:139], v[124:125]
	v_cvt_pk_f16_f32 v188, v118, v119
	v_cvt_pk_f16_f32 v189, v120, v121
	v_cvt_pk_f16_f32 v190, v122, v123
	v_cvt_pk_f16_f32 v191, v124, v125
	v_mul_f32_e32 v126, v107, v135
	v_mul_f32_e32 v127, v107, v134
	v_fma_f32 v118, v106, v134, -v126
	v_fma_f32 v119, v106, v135, v127
	v_mul_f32_e32 v126, v109, v137
	v_mul_f32_e32 v127, v109, v136
	v_fma_f32 v120, v108, v136, -v126
	v_fma_f32 v121, v108, v137, v127
	v_mul_f32_e32 v126, v103, v67
	v_mul_f32_e32 v127, v103, v66
	v_fma_f32 v122, v102, v66, -v126
	v_fma_f32 v123, v102, v67, v127
	v_mul_f32_e32 v126, v105, v69
	v_mul_f32_e32 v127, v105, v68
	v_fma_f32 v124, v104, v68, -v126
	v_fma_f32 v125, v104, v69, v127
	v_pk_mul_f32 v[118:119], v[138:139], v[118:119]
	v_pk_mul_f32 v[120:121], v[138:139], v[120:121]
	v_pk_mul_f32 v[122:123], v[138:139], v[122:123]
	v_pk_mul_f32 v[124:125], v[138:139], v[124:125]
	v_cvt_pk_f16_f32 v192, v118, v119
	v_cvt_pk_f16_f32 v193, v120, v121
	v_cvt_pk_f16_f32 v194, v122, v123
	v_cvt_pk_f16_f32 v195, v124, v125
	v_add_u32_e32 v128, 48, v146
	v_lshlrev_b32_e32 v128, 8, v128
	v_and_b32_e32 v128, 0x7ff00, v128
	v_add_u32_e32 v128, v128, v144
	global_load_dwordx4 v[66:69], v128, s[22:23] offset:16
	global_load_dwordx4 v[134:137], v128, s[22:23]
	s_waitcnt vmcnt(2)
	v_mul_f32_e32 v126, v99, v141
	v_mul_f32_e32 v127, v99, v140
	v_fma_f32 v118, v98, v140, -v126
	v_fma_f32 v119, v98, v141, v127
	v_mul_f32_e32 v126, v101, v143
	v_mul_f32_e32 v127, v101, v142
	v_fma_f32 v120, v100, v142, -v126
	v_fma_f32 v121, v100, v143, v127
	v_mul_f32_e32 v126, v95, v149
	v_mul_f32_e32 v127, v95, v148
	v_fma_f32 v122, v94, v148, -v126
	v_fma_f32 v123, v94, v149, v127
	v_mul_f32_e32 v126, v97, v151
	v_mul_f32_e32 v127, v97, v150
	v_fma_f32 v124, v96, v150, -v126
	v_fma_f32 v125, v96, v151, v127
	v_pk_mul_f32 v[118:119], v[138:139], v[118:119]
	v_pk_mul_f32 v[120:121], v[138:139], v[120:121]
	v_pk_mul_f32 v[122:123], v[138:139], v[122:123]
	v_pk_mul_f32 v[124:125], v[138:139], v[124:125]
	v_cvt_pk_f16_f32 v196, v118, v119
	v_cvt_pk_f16_f32 v197, v120, v121
	v_cvt_pk_f16_f32 v198, v122, v123
	v_cvt_pk_f16_f32 v199, v124, v125
	v_mul_f32_e32 v126, v91, v141
	v_mul_f32_e32 v127, v91, v140
	v_fma_f32 v118, v90, v140, -v126
	v_fma_f32 v119, v90, v141, v127
	v_mul_f32_e32 v126, v93, v143
	v_mul_f32_e32 v127, v93, v142
	v_fma_f32 v120, v92, v142, -v126
	v_fma_f32 v121, v92, v143, v127
	v_mul_f32_e32 v126, v87, v149
	v_mul_f32_e32 v127, v87, v148
	v_fma_f32 v122, v86, v148, -v126
	v_fma_f32 v123, v86, v149, v127
	v_mul_f32_e32 v126, v89, v151
	v_mul_f32_e32 v127, v89, v150
	v_fma_f32 v124, v88, v150, -v126
	v_fma_f32 v125, v88, v151, v127
	v_pk_mul_f32 v[118:119], v[138:139], v[118:119]
	v_pk_mul_f32 v[120:121], v[138:139], v[120:121]
	v_pk_mul_f32 v[122:123], v[138:139], v[122:123]
	v_pk_mul_f32 v[124:125], v[138:139], v[124:125]
	v_cvt_pk_f16_f32 v200, v118, v119
	v_cvt_pk_f16_f32 v201, v120, v121
	v_cvt_pk_f16_f32 v202, v122, v123
	v_cvt_pk_f16_f32 v203, v124, v125
	v_add_u32_e32 v128, 0x80, v146
	v_lshlrev_b32_e32 v128, 8, v128
	v_and_b32_e32 v128, 0x7ff00, v128
	v_add_u32_e32 v128, v128, v144
	global_load_dwordx4 v[148:151], v128, s[22:23] offset:16
	global_load_dwordx4 v[140:143], v128, s[22:23]
	s_waitcnt vmcnt(2)
	v_mul_f32_e32 v126, v83, v135
	v_mul_f32_e32 v127, v83, v134
	v_fma_f32 v118, v82, v134, -v126
	v_fma_f32 v119, v82, v135, v127
	v_mul_f32_e32 v126, v85, v137
	v_mul_f32_e32 v127, v85, v136
	v_fma_f32 v120, v84, v136, -v126
	v_fma_f32 v121, v84, v137, v127
	v_mul_f32_e32 v126, v79, v67
	v_mul_f32_e32 v127, v79, v66
	v_fma_f32 v122, v78, v66, -v126
	v_fma_f32 v123, v78, v67, v127
	v_mul_f32_e32 v126, v81, v69
	v_mul_f32_e32 v127, v81, v68
	v_fma_f32 v124, v80, v68, -v126
	v_fma_f32 v125, v80, v69, v127
	v_pk_mul_f32 v[118:119], v[138:139], v[118:119]
	v_pk_mul_f32 v[120:121], v[138:139], v[120:121]
	v_pk_mul_f32 v[122:123], v[138:139], v[122:123]
	v_pk_mul_f32 v[124:125], v[138:139], v[124:125]
	v_cvt_pk_f16_f32 v204, v118, v119
	v_cvt_pk_f16_f32 v205, v120, v121
	v_cvt_pk_f16_f32 v206, v122, v123
	v_cvt_pk_f16_f32 v207, v124, v125
	v_mul_f32_e32 v126, v75, v135
	v_mul_f32_e32 v127, v75, v134
	v_fma_f32 v118, v74, v134, -v126
	v_fma_f32 v119, v74, v135, v127
	v_mul_f32_e32 v126, v77, v137
	v_mul_f32_e32 v127, v77, v136
	v_fma_f32 v120, v76, v136, -v126
	v_fma_f32 v121, v76, v137, v127
	v_mul_f32_e32 v126, v71, v67
	v_mul_f32_e32 v127, v71, v66
	v_fma_f32 v122, v70, v66, -v126
	v_fma_f32 v123, v70, v67, v127
	v_mul_f32_e32 v126, v73, v69
	v_mul_f32_e32 v127, v73, v68
	v_fma_f32 v124, v72, v68, -v126
	v_fma_f32 v125, v72, v69, v127
	v_pk_mul_f32 v[118:119], v[138:139], v[118:119]
	v_pk_mul_f32 v[120:121], v[138:139], v[120:121]
	v_pk_mul_f32 v[122:123], v[138:139], v[122:123]
	v_pk_mul_f32 v[124:125], v[138:139], v[124:125]
	v_cvt_pk_f16_f32 v208, v118, v119
	v_cvt_pk_f16_f32 v209, v120, v121
	v_cvt_pk_f16_f32 v210, v122, v123
	v_cvt_pk_f16_f32 v211, v124, v125
	v_add_u32_e32 v128, 0x90, v146
	v_lshlrev_b32_e32 v128, 8, v128
	v_and_b32_e32 v128, 0x7ff00, v128
	v_add_u32_e32 v128, v128, v144
	global_load_dwordx4 v[66:69], v128, s[22:23] offset:16
	global_load_dwordx4 v[134:137], v128, s[22:23]
	s_waitcnt vmcnt(2)
	v_mul_f32_e32 v126, v63, v141
	v_mul_f32_e32 v127, v63, v140
	v_fma_f32 v118, v62, v140, -v126
	v_fma_f32 v119, v62, v141, v127
	v_mul_f32_e32 v126, v65, v143
	v_mul_f32_e32 v127, v65, v142
	v_fma_f32 v120, v64, v142, -v126
	v_fma_f32 v121, v64, v143, v127
	v_mul_f32_e32 v126, v59, v149
	v_mul_f32_e32 v127, v59, v148
	v_fma_f32 v122, v58, v148, -v126
	v_fma_f32 v123, v58, v149, v127
	v_mul_f32_e32 v126, v61, v151
	v_mul_f32_e32 v127, v61, v150
	v_fma_f32 v124, v60, v150, -v126
	v_fma_f32 v125, v60, v151, v127
	v_pk_mul_f32 v[118:119], v[138:139], v[118:119]
	v_pk_mul_f32 v[120:121], v[138:139], v[120:121]
	v_pk_mul_f32 v[122:123], v[138:139], v[122:123]
	v_pk_mul_f32 v[124:125], v[138:139], v[124:125]
	v_cvt_pk_f16_f32 v212, v118, v119
	v_cvt_pk_f16_f32 v213, v120, v121
	v_cvt_pk_f16_f32 v214, v122, v123
	v_cvt_pk_f16_f32 v215, v124, v125
	v_mul_f32_e32 v126, v55, v141
	v_mul_f32_e32 v127, v55, v140
	v_fma_f32 v118, v54, v140, -v126
	v_fma_f32 v119, v54, v141, v127
	v_mul_f32_e32 v126, v57, v143
	v_mul_f32_e32 v127, v57, v142
	v_fma_f32 v120, v56, v142, -v126
	v_fma_f32 v121, v56, v143, v127
	v_mul_f32_e32 v126, v51, v149
	v_mul_f32_e32 v127, v51, v148
	v_fma_f32 v122, v50, v148, -v126
	v_fma_f32 v123, v50, v149, v127
	v_mul_f32_e32 v126, v53, v151
	v_mul_f32_e32 v127, v53, v150
	v_fma_f32 v124, v52, v150, -v126
	v_fma_f32 v125, v52, v151, v127
	v_pk_mul_f32 v[118:119], v[138:139], v[118:119]
	v_pk_mul_f32 v[120:121], v[138:139], v[120:121]
	v_pk_mul_f32 v[122:123], v[138:139], v[122:123]
	v_pk_mul_f32 v[124:125], v[138:139], v[124:125]
	v_cvt_pk_f16_f32 v216, v118, v119
	v_cvt_pk_f16_f32 v217, v120, v121
	v_cvt_pk_f16_f32 v218, v122, v123
	v_cvt_pk_f16_f32 v219, v124, v125
	v_add_u32_e32 v128, 0xa0, v146
	v_lshlrev_b32_e32 v128, 8, v128
	v_and_b32_e32 v128, 0x7ff00, v128
	v_add_u32_e32 v128, v128, v144
	global_load_dwordx4 v[148:151], v128, s[22:23] offset:16
	global_load_dwordx4 v[140:143], v128, s[22:23]
	s_waitcnt vmcnt(2)
	v_mul_f32_e32 v126, v47, v135
	v_mul_f32_e32 v127, v47, v134
	v_fma_f32 v118, v46, v134, -v126
	v_fma_f32 v119, v46, v135, v127
	v_mul_f32_e32 v126, v49, v137
	v_mul_f32_e32 v127, v49, v136
	v_fma_f32 v120, v48, v136, -v126
	v_fma_f32 v121, v48, v137, v127
	v_mul_f32_e32 v126, v43, v67
	v_mul_f32_e32 v127, v43, v66
	v_fma_f32 v122, v42, v66, -v126
	v_fma_f32 v123, v42, v67, v127
	v_mul_f32_e32 v126, v45, v69
	v_mul_f32_e32 v127, v45, v68
	v_fma_f32 v124, v44, v68, -v126
	v_fma_f32 v125, v44, v69, v127
	v_pk_mul_f32 v[118:119], v[138:139], v[118:119]
	v_pk_mul_f32 v[120:121], v[138:139], v[120:121]
	v_pk_mul_f32 v[122:123], v[138:139], v[122:123]
	v_pk_mul_f32 v[124:125], v[138:139], v[124:125]
	v_cvt_pk_f16_f32 v220, v118, v119
	v_cvt_pk_f16_f32 v221, v120, v121
	v_cvt_pk_f16_f32 v222, v122, v123
	v_cvt_pk_f16_f32 v223, v124, v125
	v_mul_f32_e32 v126, v39, v135
	v_mul_f32_e32 v127, v39, v134
	v_fma_f32 v118, v38, v134, -v126
	v_fma_f32 v119, v38, v135, v127
	v_mul_f32_e32 v126, v41, v137
	v_mul_f32_e32 v127, v41, v136
	v_fma_f32 v120, v40, v136, -v126
	v_fma_f32 v121, v40, v137, v127
	v_mul_f32_e32 v126, v35, v67
	v_mul_f32_e32 v127, v35, v66
	v_fma_f32 v122, v34, v66, -v126
	v_fma_f32 v123, v34, v67, v127
	v_mul_f32_e32 v126, v37, v69
	v_mul_f32_e32 v127, v37, v68
	v_fma_f32 v124, v36, v68, -v126
	v_fma_f32 v125, v36, v69, v127
	v_pk_mul_f32 v[118:119], v[138:139], v[118:119]
	v_pk_mul_f32 v[120:121], v[138:139], v[120:121]
	v_pk_mul_f32 v[122:123], v[138:139], v[122:123]
	v_pk_mul_f32 v[124:125], v[138:139], v[124:125]
	v_cvt_pk_f16_f32 v224, v118, v119
	v_cvt_pk_f16_f32 v225, v120, v121
	v_cvt_pk_f16_f32 v226, v122, v123
	v_cvt_pk_f16_f32 v227, v124, v125
	v_add_u32_e32 v128, 0xb0, v146
	v_lshlrev_b32_e32 v128, 8, v128
	v_and_b32_e32 v128, 0x7ff00, v128
	v_add_u32_e32 v128, v128, v144
	global_load_dwordx4 v[66:69], v128, s[22:23] offset:16
	global_load_dwordx4 v[134:137], v128, s[22:23]
	s_waitcnt vmcnt(2)
	v_mul_f32_e32 v126, v31, v141
	v_mul_f32_e32 v127, v31, v140
	v_fma_f32 v118, v30, v140, -v126
	v_fma_f32 v119, v30, v141, v127
	v_mul_f32_e32 v126, v33, v143
	v_mul_f32_e32 v127, v33, v142
	v_fma_f32 v120, v32, v142, -v126
	v_fma_f32 v121, v32, v143, v127
	v_mul_f32_e32 v126, v27, v149
	v_mul_f32_e32 v127, v27, v148
	v_fma_f32 v122, v26, v148, -v126
	v_fma_f32 v123, v26, v149, v127
	v_mul_f32_e32 v126, v29, v151
	v_mul_f32_e32 v127, v29, v150
	v_fma_f32 v124, v28, v150, -v126
	v_fma_f32 v125, v28, v151, v127
	v_pk_mul_f32 v[118:119], v[138:139], v[118:119]
	v_pk_mul_f32 v[120:121], v[138:139], v[120:121]
	v_pk_mul_f32 v[122:123], v[138:139], v[122:123]
	v_pk_mul_f32 v[124:125], v[138:139], v[124:125]
	v_cvt_pk_f16_f32 v228, v118, v119
	v_cvt_pk_f16_f32 v229, v120, v121
	v_cvt_pk_f16_f32 v230, v122, v123
	v_cvt_pk_f16_f32 v231, v124, v125
	v_mul_f32_e32 v126, v23, v141
	v_mul_f32_e32 v127, v23, v140
	v_fma_f32 v118, v22, v140, -v126
	v_fma_f32 v119, v22, v141, v127
	v_mul_f32_e32 v126, v25, v143
	v_mul_f32_e32 v127, v25, v142
	v_fma_f32 v120, v24, v142, -v126
	v_fma_f32 v121, v24, v143, v127
	v_mul_f32_e32 v126, v19, v149
	v_mul_f32_e32 v127, v19, v148
	v_fma_f32 v122, v18, v148, -v126
	v_fma_f32 v123, v18, v149, v127
	v_mul_f32_e32 v126, v21, v151
	v_mul_f32_e32 v127, v21, v150
	v_fma_f32 v124, v20, v150, -v126
	v_fma_f32 v125, v20, v151, v127
	v_pk_mul_f32 v[118:119], v[138:139], v[118:119]
	v_pk_mul_f32 v[120:121], v[138:139], v[120:121]
	v_pk_mul_f32 v[122:123], v[138:139], v[122:123]
	v_pk_mul_f32 v[124:125], v[138:139], v[124:125]
	v_cvt_pk_f16_f32 v232, v118, v119
	v_cvt_pk_f16_f32 v233, v120, v121
	v_cvt_pk_f16_f32 v234, v122, v123
	v_cvt_pk_f16_f32 v235, v124, v125
	s_waitcnt vmcnt(0)
	v_mul_f32_e32 v126, v15, v135
	v_mul_f32_e32 v127, v15, v134
	v_fma_f32 v118, v14, v134, -v126
	v_fma_f32 v119, v14, v135, v127
	v_mul_f32_e32 v126, v17, v137
	v_mul_f32_e32 v127, v17, v136
	v_fma_f32 v120, v16, v136, -v126
	v_fma_f32 v121, v16, v137, v127
	v_mul_f32_e32 v126, v11, v67
	v_mul_f32_e32 v127, v11, v66
	v_fma_f32 v122, v10, v66, -v126
	v_fma_f32 v123, v10, v67, v127
	v_mul_f32_e32 v126, v13, v69
	v_mul_f32_e32 v127, v13, v68
	v_fma_f32 v124, v12, v68, -v126
	v_fma_f32 v125, v12, v69, v127
	v_pk_mul_f32 v[118:119], v[138:139], v[118:119]
	v_pk_mul_f32 v[120:121], v[138:139], v[120:121]
	v_pk_mul_f32 v[122:123], v[138:139], v[122:123]
	v_pk_mul_f32 v[124:125], v[138:139], v[124:125]
	v_cvt_pk_f16_f32 v236, v118, v119
	v_cvt_pk_f16_f32 v237, v120, v121
	v_cvt_pk_f16_f32 v238, v122, v123
	v_cvt_pk_f16_f32 v239, v124, v125
	v_mul_f32_e32 v126, v7, v135
	v_mul_f32_e32 v127, v7, v134
	v_fma_f32 v118, v6, v134, -v126
	v_fma_f32 v119, v6, v135, v127
	v_mul_f32_e32 v126, v9, v137
	v_mul_f32_e32 v127, v9, v136
	v_fma_f32 v120, v8, v136, -v126
	v_fma_f32 v121, v8, v137, v127
	v_mul_f32_e32 v126, v3, v67
	v_mul_f32_e32 v127, v3, v66
	v_fma_f32 v122, v2, v66, -v126
	v_fma_f32 v123, v2, v67, v127
	v_mul_f32_e32 v126, v5, v69
	v_mul_f32_e32 v127, v5, v68
	v_fma_f32 v124, v4, v68, -v126
	v_fma_f32 v125, v4, v69, v127
	v_pk_mul_f32 v[118:119], v[138:139], v[118:119]
	v_pk_mul_f32 v[120:121], v[138:139], v[120:121]
	v_pk_mul_f32 v[122:123], v[138:139], v[122:123]
	v_pk_mul_f32 v[124:125], v[138:139], v[124:125]
	v_cvt_pk_f16_f32 v160, v118, v119
	v_cvt_pk_f16_f32 v161, v120, v121
	v_cvt_pk_f16_f32 v162, v122, v123
	v_cvt_pk_f16_f32 v163, v124, v125
